# rowptr and dinv merged into 12-byte per-node records (one load instead of two in k_agg1/k_out)
# baseline (speedup 1.0000x reference)
.LBB1_47:
	s_or_b64 exec, exec, s[70:71]
	ds_read_b64 v[52:53], v52 offset:18432
	s_add_i32 s87, s87, 7
	s_mulk_i32 s2, 0x708
	s_and_b32 s70, s87, -8
	s_add_i32 s70, s70, s2
	s_waitcnt lgkmcnt(0)
	v_readfirstlane_b32 s71, v52
	v_readfirstlane_b32 s82, v53
	v_cmp_gt_i32_e32 vcc, s3, v36
	s_and_saveexec_b64 s[80:81], vcc
	s_cbranch_execz .LBB1_49
	v_add_u32_e32 v40, 1, v38
	v_cvt_f32_i32_e32 v40, v40
	s_mov_b32 s2, 0xf800000
	v_mul_f32_e32 v52, 0x4f800000, v40
	v_cmp_gt_f32_e32 vcc, s2, v40
	s_nop 1
	v_cndmask_b32_e32 v40, v40, v52, vcc
	v_sqrt_f32_e32 v54, v40
	v_add_u32_e32 v52, s70, v51
	v_add_u32_e32 v53, v52, v38
	v_add_u32_e32 v51, -1, v54
	v_fma_f32 v56, -v51, v54, v40
	v_add_u32_e32 v55, 1, v54
	v_cmp_ge_f32_e64 s[2:3], 0, v56
	s_nop 1
	v_cndmask_b32_e64 v51, v54, v51, s[2:3]
	v_fma_f32 v54, -v55, v54, v40
	v_cmp_lt_f32_e64 s[2:3], 0, v54
	s_nop 1
	v_cndmask_b32_e64 v51, v51, v55, s[2:3]
	v_mul_f32_e32 v54, 0x37800000, v51
	v_cndmask_b32_e32 v51, v51, v54, vcc
	v_mov_b32_e32 v54, 0x260
	v_cmp_class_f32_e32 vcc, v40, v54
	v_mad_u64_u32 v[54:55], s[88:89], v36, 12, s[72:73]
	v_mov_b32_e32 v58, v54
	v_mov_b32_e32 v59, v55
	global_store_dwordx2 v[54:55], v[52:53], off
	v_cndmask_b32_e32 v40, v51, v40, vcc
	v_div_scale_f32 v51, s[2:3], v40, v40, 1.0
	v_rcp_f32_e32 v56, v51
	s_mov_b32 s72, 0
	s_mov_b32 s73, s72
	v_fma_f32 v52, -v51, v56, 1.0
	v_fmac_f32_e32 v56, v52, v56
	v_div_scale_f32 v52, vcc, 1.0, v40, 1.0
	v_mul_f32_e32 v53, v52, v56
	v_fma_f32 v54, -v51, v53, v52
	v_fmac_f32_e32 v53, v54, v56
	v_fma_f32 v51, -v51, v53, v52
	v_div_fmas_f32 v51, v51, v56, v53
	v_div_fixup_f32 v40, v51, v40, 1.0
	global_store_dword v[58:59], v40, off offset:8
	v_lshlrev_b64 v[36:37], 5, v[36:37]
	s_mov_b32 s74, s72
	s_mov_b32 s75, s72
	v_mov_b64_e32 v[52:53], s[72:73]
	v_lshl_add_u64 v[36:37], s[78:79], 0, v[36:37]
	v_mov_b64_e32 v[54:55], s[74:75]
	global_store_dwordx4 v[36:37], v[52:55], off
	global_store_dwordx4 v[36:37], v[52:55], off offset:16

	.amdhsa_kernel _Z5k_csrPKiPKjP15HIP_vector_typeIiLj2EEPfPtS6_
		.amdhsa_group_segment_fixed_size 18452
		.amdhsa_private_segment_fixed_size 0
		.amdhsa_kernarg_size 48
		.amdhsa_user_sgpr_count 2
		.amdhsa_user_sgpr_dispatch_ptr 0
		.amdhsa_user_sgpr_queue_ptr 0
		.amdhsa_user_sgpr_kernarg_segment_ptr 1
		.amdhsa_user_sgpr_dispatch_id 0
		.amdhsa_user_sgpr_kernarg_preload_length 0
		.amdhsa_user_sgpr_kernarg_preload_offset 0
		.amdhsa_user_sgpr_private_segment_size 0
		.amdhsa_uses_dynamic_stack 0
		.amdhsa_enable_private_segment 0
		.amdhsa_system_sgpr_workgroup_id_x 1
		.amdhsa_system_sgpr_workgroup_id_y 0
		.amdhsa_system_sgpr_workgroup_id_z 0
		.amdhsa_system_sgpr_workgroup_info 0
		.amdhsa_system_vgpr_workitem_id 0
		.amdhsa_next_free_vgpr 65
		.amdhsa_next_free_sgpr 90
		.amdhsa_accum_offset 68
		.amdhsa_reserve_vcc 1
		.amdhsa_float_round_mode_32 0
		.amdhsa_float_round_mode_16_64 0
		.amdhsa_float_denorm_mode_32 3
		.amdhsa_float_denorm_mode_16_64 3
		.amdhsa_dx10_clamp 1
		.amdhsa_ieee_mode 1
		.amdhsa_fp16_overflow 0
		.amdhsa_tg_split 0
		.amdhsa_exception_fp_ieee_invalid_op 0
		.amdhsa_exception_fp_denorm_src 0
		.amdhsa_exception_fp_ieee_div_zero 0
		.amdhsa_exception_fp_ieee_overflow 0
		.amdhsa_exception_fp_ieee_underflow 0
		.amdhsa_exception_fp_ieee_inexact 0
		.amdhsa_exception_int_div_zero 0
	.end_amdhsa_kernel

_Z6k_gemmPKfPKDv8_DF16_S0_S0_PDF16_:
	s_load_dwordx2 s[8:9], s[0:1], 0x0
	s_load_dwordx2 s[10:11], s[0:1], 0x10
	s_load_dwordx2 s[12:13], s[0:1], 0x8
	s_load_dwordx4 s[4:7], s[0:1], 0x18
	s_mul_i32 s14, s2, 0xc4
	v_lshrrev_b32_e32 v1, 5, v0
	v_and_b32_e32 v89, 31, v0
	v_add_u32_e32 v2, s14, v1
	v_lshlrev_b32_e32 v154, 4, v89
	s_movk_i32 s15, 0x1664
	v_mad_u64_u32 v[150:151], s[0:1], v2, s15, v[154:155]
	s_lshl_b32 s16, s2, 2
	v_mul_u32_u24_e32 v245, 25, v1
	v_add_u32_e32 v245, s16, v245
	v_and_b32_e32 v245, 31, v245
	v_xor_b32_e32 v246, 16, v245
	v_lshlrev_b32_e32 v247, 2, v246
	v_sub_u32_e32 v244, v150, v247
	v_lshlrev_b32_e32 v247, 2, v245
	v_sub_u32_e32 v150, v150, v247
	v_add_u32_e32 v247, 24, v245
	v_lshrrev_b32_e32 v247, 2, v247
	v_sub_u32_e32 v247, v89, v247
	v_max_i32_e32 v247, 0, v247
	v_lshlrev_b32_e32 v247, 4, v247
	v_sub_u32_e32 v250, v150, v247
	v_add_u32_e32 v247, 24, v246
	v_lshrrev_b32_e32 v247, 2, v247
	v_sub_u32_e32 v247, v89, v247
	v_max_i32_e32 v247, 0, v247
	v_lshlrev_b32_e32 v247, 4, v247
	v_sub_u32_e32 v251, v244, v247
	s_movk_i32 s17, 0x1ee0
	v_mul_u32_u24_e32 v242, s17, v1
	v_add_u32_e32 v243, 0xffffff00, v242
	v_lshl_add_u32 v247, v89, 3, v242
	v_lshlrev_b32_e32 v248, 1, v245
	v_sub_u32_e32 v248, v247, v248
	v_add_u32_e32 v234, 64, v248
	v_add_u32_e32 v235, 0x42, v248
	v_add_u32_e32 v236, 0x44, v248
	v_add_u32_e32 v237, 0x46, v248
	v_lshlrev_b32_e32 v248, 1, v246
	v_sub_u32_e32 v248, v247, v248
	v_add_u32_e32 v238, 64, v248
	v_add_u32_e32 v239, 0x42, v248
	v_add_u32_e32 v240, 0x44, v248
	v_add_u32_e32 v241, 0x46, v248
	v_and_b32_e32 v247, 7, v89
	v_lshl_add_u32 v247, v247, 3, v242
	v_mov_b32_e32 v248, 0
	v_mov_b32_e32 v249, 0
	ds_write_b64 v247, v[248:249] offset:0
	ds_write_b64 v247, v[248:249] offset:608
	ds_write_b64 v247, v[248:249] offset:1216
	ds_write_b64 v247, v[248:249] offset:1824
	ds_write_b64 v247, v[248:249] offset:2432
	ds_write_b64 v247, v[248:249] offset:3040
	ds_write_b64 v247, v[248:249] offset:3648
	ds_write_b64 v247, v[248:249] offset:4256
	ds_write_b64 v247, v[248:249] offset:4864
	ds_write_b64 v247, v[248:249] offset:5472
	ds_write_b64 v247, v[248:249] offset:6080
	ds_write_b64 v247, v[248:249] offset:6688
	ds_write_b64 v247, v[248:249] offset:7296
	v_mov_b32_e32 v2, 2
	v_lshlrev_b32_sdwa v2, v2, v0 dst_sel:DWORD dst_unused:UNUSED_PAD src0_sel:DWORD src1_sel:BYTE_0
	v_mov_b32_e32 v3, 0
	s_waitcnt lgkmcnt(0)
	v_lshl_add_u64 v[4:5], s[4:5], 0, v[2:3]
	s_mov_b32 s0, 0x166000
	v_add_co_u32_e32 v4, vcc, s0, v4
	v_add_u32_e32 v6, 0x111514dc, v154
	s_nop 0
	v_addc_co_u32_e32 v5, vcc, 0, v5, vcc
	global_load_dword v90, v[4:5], off
	v_add_u32_e32 v4, 0x16640, v244
	v_min_u32_e32 v2, v150, v6
	v_min_u32_e32 v4, v4, v6
	global_load_dwordx4 v[82:85], v2, s[8:9] nt
	global_load_dwordx4 v[78:81], v4, s[8:9] nt
	v_add_u32_e32 v2, 0x2cc80, v150
	v_min_u32_e32 v2, v2, v6
	v_add_u32_e32 v4, 0x432c0, v244
	v_min_u32_e32 v4, v4, v6
	global_load_dwordx4 v[74:77], v2, s[8:9] nt
	global_load_dwordx4 v[70:73], v4, s[8:9] nt
	v_add_u32_e32 v2, 0x59900, v150
	v_min_u32_e32 v2, v2, v6
	v_add_u32_e32 v4, 0x6ff40, v244
	v_min_u32_e32 v4, v4, v6
	global_load_dwordx4 v[66:69], v2, s[8:9] nt
	global_load_dwordx4 v[54:57], v4, s[8:9] nt
	v_add_u32_e32 v2, 0x86580, v150
	v_min_u32_e32 v2, v2, v6
	v_add_u32_e32 v4, 0x9cbc0, v244
	v_min_u32_e32 v4, v4, v6
	global_load_dwordx4 v[62:65], v2, s[8:9] nt
	global_load_dwordx4 v[58:61], v4, s[8:9] nt
	v_add_u32_e32 v2, 0xb3200, v150
	v_min_u32_e32 v2, v2, v6
	v_add_u32_e32 v4, 0xc9840, v244
	v_min_u32_e32 v4, v4, v6
	global_load_dwordx4 v[46:49], v2, s[8:9] nt
	global_load_dwordx4 v[38:41], v4, s[8:9] nt
	v_add_u32_e32 v2, 0xdfe80, v150
	v_min_u32_e32 v2, v2, v6
	v_add_u32_e32 v4, 0xf64c0, v244
	s_movk_i32 s3, 0xc4
	v_or_b32_e32 v7, 0xc0, v1
	v_min_u32_e32 v4, v4, v6
	global_load_dwordx4 v[34:37], v2, s[8:9] nt
	global_load_dwordx4 v[14:17], v4, s[8:9] nt
	v_add_u32_e32 v2, 0x10cb00, v150
	v_min_u32_e32 v2, v2, v6
	v_cmp_gt_u32_e64 s[0:1], s3, v7
	v_bfe_u32 v87, v0, 4, 2
	v_and_b32_e32 v86, 15, v0
	v_cndmask_b32_e64 v2, 0, v2, s[0:1]
	global_load_dwordx4 v[10:13], v2, s[8:9] nt
	v_lshlrev_b32_e32 v2, 12, v87
	v_lshl_add_u64 v[4:5], s[12:13], 0, v[2:3]
	v_lshlrev_b32_e32 v2, 3, v0
	v_and_b32_e32 v2, 0xe00, v2
	v_lshl_add_u64 v[4:5], v[4:5], 0, v[2:3]
	v_lshlrev_b32_e32 v2, 4, v86
	v_lshl_add_u64 v[152:153], v[4:5], 0, v[2:3]
	s_movk_i32 s2, 0x4000
	v_add_co_u32_e32 v2, vcc, s2, v152
	s_mov_b32 s2, 0x8000
	s_nop 0
	v_addc_co_u32_e32 v3, vcc, 0, v153, vcc
	global_load_dwordx4 v[26:29], v[152:153], off sc1
	global_load_dwordx4 v[50:53], v[152:153], off offset:256 sc1
	global_load_dwordx4 v[18:21], v[2:3], off sc1
	global_load_dwordx4 v[42:45], v[2:3], off offset:256 sc1
	v_add_co_u32_e32 v2, vcc, s2, v152
	s_movk_i32 s2, 0xd0
	s_nop 0
	v_addc_co_u32_e32 v3, vcc, 0, v153, vcc
	v_add_co_u32_e32 v92, vcc, 0xc000, v152
	global_load_dwordx4 v[22:25], v[2:3], off sc1
	global_load_dwordx4 v[30:33], v[2:3], off offset:256 sc1
	v_addc_co_u32_e32 v93, vcc, 0, v153, vcc
	global_load_dwordx4 v[6:9], v[92:93], off sc1
	global_load_dwordx4 v[2:5], v[92:93], off offset:256 sc1
	v_cmp_gt_u32_e32 vcc, s2, v0
	v_add_u32_e32 v88, 0x111516dc, v154
	s_and_saveexec_b64 s[4:5], vcc
	s_cbranch_execz .LBB2_5
	v_cndmask_b32_e32 v91, 0, v0, vcc
	v_cmp_gt_u32_e32 vcc, s3, v91
	v_add_u32_e32 v91, s14, v91
	s_mov_b32 s2, 0xc350
	v_cmp_gt_i32_e64 s[2:3], s2, v91
	v_ashrrev_i32_e32 v92, 31, v91
	s_and_b64 s[2:3], vcc, s[2:3]
	v_cndmask_b32_e64 v93, 0, v92, s[2:3]
	v_mov_b32_e32 v92, 0xc34f
	v_cndmask_b32_e64 v92, v92, v91, s[2:3]
	v_mov_b64_e32 v[94:95], s[8:9]
	v_mad_i64_i32 v[94:95], s[12:13], v92, s15, v[94:95]
	v_add_co_u32_e32 v94, vcc, 0x1000, v94
	s_sub_u32 s10, s10, 0x61af8
	s_subb_u32 s11, s11, 0
	v_mad_u64_u32 v[92:93], s[18:19], v92, 12, s[10:11]
	s_nop 0
	v_addc_co_u32_e32 v95, vcc, 0, v95, vcc
	global_load_dword v252, v[92:93], off
	global_load_dword v253, v[94:95], off offset:1632
	s_mov_b64 s[18:19], s[2:3]

.LBB3_2:
	s_mul_i32 s18, s33, 0x4e2
	v_add_u32_e32 v0, s18, v8
	v_lshl_or_b32 v4, v0, 3, v21
	v_lshl_or_b32 v0, v4, 7, v6
	global_load_dwordx4 v[30:33], v0, s[20:21]
	v_mad_u64_u32 v[2:3], s[18:19], v4, 12, s[22:23]
	global_load_dwordx3 v[0:2], v[2:3], off
	s_waitcnt vmcnt(1)
	v_cvt_f32_f16_e32 v18, v30
	v_cvt_f32_f16_sdwa v19, v30 dst_sel:DWORD dst_unused:UNUSED_PAD src0_sel:WORD_1
	v_cvt_f32_f16_e32 v16, v31
	v_cvt_f32_f16_sdwa v17, v31 dst_sel:DWORD dst_unused:UNUSED_PAD src0_sel:WORD_1
	v_cvt_f32_f16_e32 v14, v32
	v_cvt_f32_f16_sdwa v15, v32 dst_sel:DWORD dst_unused:UNUSED_PAD src0_sel:WORD_1
	v_cvt_f32_f16_e32 v12, v33
	v_cvt_f32_f16_sdwa v13, v33 dst_sel:DWORD dst_unused:UNUSED_PAD src0_sel:WORD_1
	s_waitcnt vmcnt(0)
	v_mov_b32_e32 v29, v2
	v_cmp_lt_i32_e64 s[18:19], v0, v1
	s_and_saveexec_b64 s[28:29], s[18:19]
	s_cbranch_execz .LBB3_6
	v_ashrrev_i32_e32 v3, 31, v0
	v_mov_b32_e32 v2, v0
	v_lshl_add_u64 v[2:3], v[2:3], 1, s[24:25]
	s_mov_b64 s[30:31], 0

_Z5k_outPKfPK15HIP_vector_typeIiLj2EEPKtS0_S0_Pf:
	v_lshl_or_b32 v6, s2, 8, v0
	v_ashrrev_i32_e32 v2, 3, v6
	s_mov_b32 s2, 0xc350
	v_cmp_gt_i32_e32 vcc, s2, v2
	s_and_saveexec_b64 s[2:3], vcc
	s_cbranch_execz .LBB4_7
	s_load_dwordx4 s[4:7], s[0:1], 0x0
	s_load_dwordx4 s[8:11], s[0:1], 0x18
	v_and_b32_e32 v0, 7, v0
	v_ashrrev_i32_e32 v3, 31, v2
	v_ashrrev_i32_e32 v7, 31, v6
	v_cmp_ne_u32_e32 vcc, 7, v0
	s_waitcnt lgkmcnt(0)
	v_lshl_add_u64 v[6:7], v[6:7], 2, s[4:5]
	v_cndmask_b32_e32 v1, 0, v0, vcc
	global_load_dword v8, v[6:7], off
	v_mad_u64_u32 v[4:5], s[12:13], v2, 12, s[6:7]
	v_lshlrev_b32_e32 v1, 2, v1
	global_load_dwordx3 v[4:6], v[4:5], off
	global_load_dword v3, v1, s[10:11]
	s_load_dwordx2 s[6:7], s[0:1], 0x28
	s_waitcnt vmcnt(1)
	v_mov_b32_e32 v9, v6
	v_cmp_lt_i32_e64 s[2:3], v4, v5
	s_and_saveexec_b64 s[8:9], s[2:3]
	s_cbranch_execz .LBB4_5
	s_load_dwordx2 s[0:1], s[0:1], 0x10
	v_ashrrev_i32_e32 v7, 31, v4
	v_mov_b32_e32 v6, v4
	v_mov_b32_e32 v1, v0
	s_mov_b64 s[2:3], 0
	s_waitcnt lgkmcnt(0)
	v_lshl_add_u64 v[6:7], v[6:7], 1, s[0:1]
	v_mov_b32_e32 v10, 3

	.amdhsa_kernel _Z5k_outPKfPK15HIP_vector_typeIiLj2EEPKtS0_S0_Pf
		.amdhsa_group_segment_fixed_size 0
		.amdhsa_private_segment_fixed_size 0
		.amdhsa_kernarg_size 48
		.amdhsa_user_sgpr_count 2
		.amdhsa_user_sgpr_dispatch_ptr 0
		.amdhsa_user_sgpr_queue_ptr 0
		.amdhsa_user_sgpr_kernarg_segment_ptr 1
		.amdhsa_user_sgpr_dispatch_id 0
		.amdhsa_user_sgpr_kernarg_preload_length 0
		.amdhsa_user_sgpr_kernarg_preload_offset 0
		.amdhsa_user_sgpr_private_segment_size 0
		.amdhsa_uses_dynamic_stack 0
		.amdhsa_enable_private_segment 0
		.amdhsa_system_sgpr_workgroup_id_x 1
		.amdhsa_system_sgpr_workgroup_id_y 0
		.amdhsa_system_sgpr_workgroup_id_z 0
		.amdhsa_system_sgpr_workgroup_info 0
		.amdhsa_system_vgpr_workitem_id 0
		.amdhsa_next_free_vgpr 27
		.amdhsa_next_free_sgpr 14
		.amdhsa_accum_offset 28
		.amdhsa_reserve_vcc 1
		.amdhsa_float_round_mode_32 0
		.amdhsa_float_round_mode_16_64 0
		.amdhsa_float_denorm_mode_32 3
		.amdhsa_float_denorm_mode_16_64 3
		.amdhsa_dx10_clamp 1
		.amdhsa_ieee_mode 1
		.amdhsa_fp16_overflow 0
		.amdhsa_tg_split 0
		.amdhsa_exception_fp_ieee_invalid_op 0
		.amdhsa_exception_fp_denorm_src 0
		.amdhsa_exception_fp_ieee_div_zero 0
		.amdhsa_exception_fp_ieee_overflow 0
		.amdhsa_exception_fp_ieee_underflow 0
		.amdhsa_exception_fp_ieee_inexact 0
		.amdhsa_exception_int_div_zero 0
	.end_amdhsa_kernel

amdhsa.kernels:
  - .agpr_count:     0
    .args:
      - .actual_access:  read_only
        .address_space:  global
        .offset:         0
        .size:           8
        .value_kind:     global_buffer
      - .actual_access:  write_only
        .address_space:  global
        .offset:         8
        .size:           8
        .value_kind:     global_buffer
      - .actual_access:  write_only
        .address_space:  global
        .offset:         16
        .size:           8
        .value_kind:     global_buffer
      - .actual_access:  read_only
        .address_space:  global
        .offset:         24
        .size:           8
        .value_kind:     global_buffer
      - .actual_access:  write_only
        .address_space:  global
        .offset:         32
        .size:           8
        .value_kind:     global_buffer
      - .actual_access:  write_only
        .address_space:  global
        .offset:         40
        .size:           8
        .value_kind:     global_buffer
    .group_segment_fixed_size: 14576
    .kernarg_segment_align: 8
    .kernarg_segment_size: 48
    .language:       OpenCL C
    .language_version:
      - 2
      - 0
    .max_flat_workgroup_size: 256
    .name:           _Z5k_binPKiPiPjPKfPDv8_DF16_PDF16_
    .private_segment_fixed_size: 0
    .sgpr_count:     22
    .sgpr_spill_count: 0
    .symbol:         _Z5k_binPKiPiPjPKfPDv8_DF16_PDF16_.kd
    .uniform_work_group_size: 1
    .uses_dynamic_stack: false
    .vgpr_count:     75
    .vgpr_spill_count: 0
    .wavefront_size: 64
  - .agpr_count:     0
    .args:
      - .actual_access:  read_only
        .address_space:  global
        .offset:         0
        .size:           8
        .value_kind:     global_buffer
      - .actual_access:  read_only
        .address_space:  global
        .offset:         8
        .size:           8
        .value_kind:     global_buffer
      - .actual_access:  write_only
        .address_space:  global
        .offset:         16
        .size:           8
        .value_kind:     global_buffer
      - .actual_access:  write_only
        .address_space:  global
        .offset:         24
        .size:           8
        .value_kind:     global_buffer
      - .actual_access:  write_only
        .address_space:  global
        .offset:         32
        .size:           8
        .value_kind:     global_buffer
      - .actual_access:  write_only
        .address_space:  global
        .offset:         40
        .size:           8
        .value_kind:     global_buffer
    .group_segment_fixed_size: 18452
    .kernarg_segment_align: 8
    .kernarg_segment_size: 48
    .language:       OpenCL C
    .language_version:
      - 2
      - 0
    .max_flat_workgroup_size: 256
    .name:           _Z5k_csrPKiPKjP15HIP_vector_typeIiLj2EEPfPtS6_
    .private_segment_fixed_size: 0
    .sgpr_count:     96
    .sgpr_spill_count: 0
    .symbol:         _Z5k_csrPKiPKjP15HIP_vector_typeIiLj2EEPfPtS6_.kd
    .uniform_work_group_size: 1
    .uses_dynamic_stack: false
    .vgpr_count:     65
    .vgpr_spill_count: 0
    .wavefront_size: 64
  - .agpr_count:     0
    .args:
      - .actual_access:  read_only
        .address_space:  global
        .offset:         0
        .size:           8
        .value_kind:     global_buffer
      - .actual_access:  read_only
        .address_space:  global
        .offset:         8
        .size:           8
        .value_kind:     global_buffer
      - .actual_access:  read_only
        .address_space:  global
        .offset:         16
        .size:           8
        .value_kind:     global_buffer
      - .actual_access:  read_only
        .address_space:  global
        .offset:         24
        .size:           8
        .value_kind:     global_buffer
      - .actual_access:  write_only
        .address_space:  global
        .offset:         32
        .size:           8
        .value_kind:     global_buffer
    .group_segment_fixed_size: 129152
    .kernarg_segment_align: 8
    .kernarg_segment_size: 40
    .language:       OpenCL C
    .language_version:
      - 2
      - 0
    .max_flat_workgroup_size: 512
    .name:           _Z6k_gemmPKfPKDv8_DF16_S0_S0_PDF16_
    .private_segment_fixed_size: 0
    .sgpr_count:     22
    .sgpr_spill_count: 0
    .symbol:         _Z6k_gemmPKfPKDv8_DF16_S0_S0_PDF16_.kd
    .uniform_work_group_size: 1
    .uses_dynamic_stack: false
    .vgpr_count:     256
    .vgpr_spill_count: 0
    .wavefront_size: 64
  - .agpr_count:     0
    .args:
      - .actual_access:  read_only
        .address_space:  global
        .offset:         0
        .size:           8
        .value_kind:     global_buffer
      - .actual_access:  read_only
        .address_space:  global
        .offset:         8
        .size:           8
        .value_kind:     global_buffer
      - .actual_access:  read_only
        .address_space:  global
        .offset:         16
        .size:           8
        .value_kind:     global_buffer
      - .actual_access:  read_only
        .address_space:  global
        .offset:         24
        .size:           8
        .value_kind:     global_buffer
      - .actual_access:  read_only
        .address_space:  global
        .offset:         32
        .size:           8
        .value_kind:     global_buffer
      - .actual_access:  read_only
        .address_space:  global
        .offset:         40
        .size:           8
        .value_kind:     global_buffer
      - .address_space:  global
        .offset:         48
        .size:           8
        .value_kind:     global_buffer
    .group_segment_fixed_size: 2304
    .kernarg_segment_align: 8
    .kernarg_segment_size: 56
    .language:       OpenCL C
    .language_version:
      - 2
      - 0
    .max_flat_workgroup_size: 320
    .name:           _Z6k_agg1PKDF16_PK15HIP_vector_typeIiLj2EEPKtPKfS8_S8_Pf
    .private_segment_fixed_size: 0
    .sgpr_count:     40
    .sgpr_spill_count: 0
    .symbol:         _Z6k_agg1PKDF16_PK15HIP_vector_typeIiLj2EEPKtPKfS8_S8_Pf.kd
    .uniform_work_group_size: 1
    .uses_dynamic_stack: false
    .vgpr_count:     63
    .vgpr_spill_count: 0
    .wavefront_size: 64
  - .agpr_count:     0
    .args:
      - .actual_access:  read_only
        .address_space:  global
        .offset:         0
        .size:           8
        .value_kind:     global_buffer
      - .actual_access:  read_only
        .address_space:  global
        .offset:         8
        .size:           8
        .value_kind:     global_buffer
      - .actual_access:  read_only
        .address_space:  global
        .offset:         16
        .size:           8
        .value_kind:     global_buffer
      - .actual_access:  read_only
        .address_space:  global
        .offset:         24
        .size:           8
        .value_kind:     global_buffer
      - .actual_access:  read_only
        .address_space:  global
        .offset:         32
        .size:           8
        .value_kind:     global_buffer
      - .actual_access:  write_only
        .address_space:  global
        .offset:         40
        .size:           8
        .value_kind:     global_buffer
    .group_segment_fixed_size: 0
    .kernarg_segment_align: 8
    .kernarg_segment_size: 48
    .language:       OpenCL C
    .language_version:
      - 2
      - 0
    .max_flat_workgroup_size: 256
    .name:           _Z5k_outPKfPK15HIP_vector_typeIiLj2EEPKtS0_S0_Pf
    .private_segment_fixed_size: 0
    .sgpr_count:     20
    .sgpr_spill_count: 0
    .symbol:         _Z5k_outPKfPK15HIP_vector_typeIiLj2EEPKtS0_S0_Pf.kd
    .uniform_work_group_size: 1
    .uses_dynamic_stack: false
    .vgpr_count:     27
    .vgpr_spill_count: 0
    .wavefront_size: 64
